# prep: weight-folding blocks take the lowest block ids (dispatched first), conversion blocks after (XCD alignment kept)
# speedup vs baseline: 1.0146x; 1.0146x over previous
_Z7na_prepPKfS0_S0_S0_S0_S0_PDF16_PhS1_PfS3_S3_:
	s_cmpk_lt_u32 s2, 0x88
	s_cbranch_scc0 .Lremap_b
	s_addk_i32 s2, 0x100
	s_branch .Lremap_done
.Lremap_b:
	s_cmpk_lt_u32 s2, 0x188
	s_cbranch_scc0 .Lremap_done
	s_addk_i32 s2, 0xff78
.Lremap_done:
	s_cmpk_gt_u32 s2, 0xff
	s_mov_b64 s[4:5], -1
	s_cbranch_scc1 .LBB0_3
	s_andn2_b64 vcc, exec, s[4:5]
	s_cbranch_vccz .LBB0_39
